# v038 + grid barrier: buffer_inv sc1 issued before the poll loops instead of after the flag (L1 stays empty while the WG is parked)
# speedup vs baseline: 1.0096x; 1.0096x over previous
; __device__ __forceinline__ unsigned xb_ld(unsigned* p)              { return __hip_atomic_load(p, __ATOMIC_RELAXED, __HIP_MEMORY_SCOPE_AGENT); }
; __device__ __forceinline__ unsigned xb_add(unsigned* p, unsigned v) { return __hip_atomic_fetch_add(p, v, __ATOMIC_RELAXED, __HIP_MEMORY_SCOPE_AGENT); }
; #define XB_SPIN(cond, bar) do { unsigned _sp = 0; while (cond) { __builtin_amdgcn_s_sleep(1); \
;     if ((++_sp & 255u) == 0u) { if (xb_ld(&(bar)[XB_TMO])) break; if (_sp > XB_SPIN_CAP) { atomicAdd(&(bar)[XB_TMO], 1u); break; } } } } while (0)
; __device__ __forceinline__ void xcd_barrier(const XcdBarrier& b) {
;     ...
;         unsigned nloc = b.st[0], nx = b.st[1];
;         if (nloc == 0u) { xcd_barrier_complete(bar, b.x, nloc, nx); b.st[0] = nloc; b.st[1] = nx; }
;         const unsigned old = xb_add(&bar[XB_XSUB(b.x)], 1u);
;         const unsigned gen = old / nloc;
;         if (old + 1u == (gen + 1u) * nloc) {
;             __builtin_amdgcn_fence(__ATOMIC_RELEASE, "agent");
;             asm volatile("s_waitcnt vmcnt(0)" ::: "memory");
;             const unsigned og = xb_add(&bar[XB_TOP], 1u);
;             const unsigned tg = og / nx;
;             if (og + 1u == (tg + 1u) * nx) xb_add(&bar[XB_TOPGEN], 1u);
;             else XB_SPIN(xb_ld(&bar[XB_TOPGEN]) == tg, bar);
;             __builtin_amdgcn_fence(__ATOMIC_ACQUIRE, "agent");
;             xb_add(&bar[XB_XGEN(b.x)], 1u);
;             asm volatile("s_waitcnt vmcnt(0)" ::: "memory");
;         } else {
;             XB_SPIN(xb_ld(&bar[XB_XGEN(b.x)]) == gen, bar);
.LBB0_80:
	s_or_b64 exec, exec, s[10:11]
	v_cvt_f32_u32_e32 v5, v3
	s_waitcnt vmcnt(0)
	v_readfirstlane_b32 s3, v4
	v_sub_u32_e32 v4, 0, v3
	v_rcp_iflag_f32_e32 v5, v5
	v_add_u32_e32 v6, s3, v2
	v_mul_f32_e32 v5, 0x4f7ffffe, v5
	v_cvt_u32_f32_e32 v5, v5
	v_mul_lo_u32 v2, v4, v5
	v_mul_hi_u32 v2, v5, v2
	v_add_u32_e32 v2, v5, v2
	v_mul_hi_u32 v2, v6, v2
	v_mul_lo_u32 v4, v2, v3
	v_sub_u32_e32 v4, v6, v4
	v_add_u32_e32 v5, 1, v2
	v_cmp_ge_u32_e32 vcc, v4, v3
	s_nop 1
	v_cndmask_b32_e32 v2, v2, v5, vcc
	v_sub_u32_e32 v5, v4, v3
	v_cndmask_b32_e32 v4, v4, v5, vcc
	v_add_u32_e32 v5, 1, v2
	v_cmp_ge_u32_e32 vcc, v4, v3
	v_add_u32_e32 v4, 1, v6
	s_nop 0
	v_cndmask_b32_e32 v2, v2, v5, vcc
	v_mul_lo_u32 v5, v3, v2
	v_add_u32_e32 v3, v5, v3
	v_cmp_ne_u32_e32 vcc, v4, v3
	s_and_saveexec_b64 s[8:9], vcc
	s_xor_b64 s[8:9], exec, s[8:9]
	s_cbranch_execz .LBB0_94
	s_waitcnt lgkmcnt(0)
	buffer_inv sc1
	v_mov_b32_e32 v1, 0x2000
	global_load_dword v1, v1, s[6:7] offset:1024 sc1
	s_add_u32 s12, s6, 0x2400
	s_addc_u32 s13, s7, 0
	s_waitcnt vmcnt(0)
	v_cmp_eq_u32_e32 vcc, v1, v2
	s_and_saveexec_b64 s[10:11], vcc
	s_cbranch_execz .LBB0_93
	s_mov_b32 s3, 1
	s_mov_b64 s[14:15], 0
	v_mov_b32_e32 v1, 0
	s_branch .LBB0_84

; __device__ __forceinline__ unsigned xb_ld(unsigned* p)              { return __hip_atomic_load(p, __ATOMIC_RELAXED, __HIP_MEMORY_SCOPE_AGENT); }
; #define XB_SPIN(cond, bar) do { unsigned _sp = 0; while (cond) { __builtin_amdgcn_s_sleep(1); \
;     if ((++_sp & 255u) == 0u) { if (xb_ld(&(bar)[XB_TMO])) break; if (_sp > XB_SPIN_CAP) { atomicAdd(&(bar)[XB_TMO], 1u); break; } } } } while (0)
; __device__ __forceinline__ void xcd_barrier(const XcdBarrier& b) {
;     ...
;             XB_SPIN(xb_ld(&bar[XB_XGEN(b.x)]) == gen, bar);
;             __builtin_amdgcn_fence(__ATOMIC_ACQUIRE, "agent");
;             asm volatile("s_waitcnt vmcnt(0)" ::: "memory");
.LBB0_93:
	s_or_b64 exec, exec, s[10:11]
	s_waitcnt vmcnt(0)
	s_waitcnt vmcnt(0)

; __device__ __forceinline__ unsigned xb_ld(unsigned* p)              { return __hip_atomic_load(p, __ATOMIC_RELAXED, __HIP_MEMORY_SCOPE_AGENT); }
; __device__ __forceinline__ unsigned xb_add(unsigned* p, unsigned v) { return __hip_atomic_fetch_add(p, v, __ATOMIC_RELAXED, __HIP_MEMORY_SCOPE_AGENT); }
; #define XB_SPIN(cond, bar) do { unsigned _sp = 0; while (cond) { __builtin_amdgcn_s_sleep(1); \
;     if ((++_sp & 255u) == 0u) { if (xb_ld(&(bar)[XB_TMO])) break; if (_sp > XB_SPIN_CAP) { atomicAdd(&(bar)[XB_TMO], 1u); break; } } } } while (0)
; __device__ __forceinline__ void xcd_barrier(const XcdBarrier& b) {
;     ...
;             const unsigned og = xb_add(&bar[XB_TOP], 1u);
;             const unsigned tg = og / nx;
;             if (og + 1u == (tg + 1u) * nx) xb_add(&bar[XB_TOPGEN], 1u);
;             else XB_SPIN(xb_ld(&bar[XB_TOPGEN]) == tg, bar);
.LBB0_97:
	s_or_b64 exec, exec, s[10:11]
	buffer_inv sc1
	v_cvt_f32_u32_e32 v4, v1
	s_waitcnt vmcnt(0)
	v_readfirstlane_b32 s3, v3
	s_add_u32 s10, s90, 0x3500
	s_addc_u32 s11, s91, 0
	v_rcp_iflag_f32_e32 v4, v4
	v_add_u32_e32 v2, s3, v2
	v_add_u32_e32 v5, 1, v2
	s_mov_b64 s[12:13], -1
	v_mul_f32_e32 v3, 0x4f7ffffe, v4
	v_cvt_u32_f32_e32 v3, v3
	v_sub_u32_e32 v4, 0, v1
	v_mul_lo_u32 v4, v4, v3
	v_mul_hi_u32 v4, v3, v4
	v_add_u32_e32 v3, v3, v4
	v_mul_hi_u32 v3, v2, v3
	v_mul_lo_u32 v4, v3, v1
	v_sub_u32_e32 v2, v2, v4
	v_add_u32_e32 v6, 1, v3
	v_cmp_ge_u32_e32 vcc, v2, v1
	v_sub_u32_e32 v4, v2, v1
	s_nop 0
	v_cndmask_b32_e32 v3, v3, v6, vcc
	v_cndmask_b32_e32 v2, v2, v4, vcc
	v_add_u32_e32 v4, 1, v3
	v_cmp_ge_u32_e32 vcc, v2, v1
	s_nop 1
	v_cndmask_b32_e32 v4, v3, v4, vcc
	v_mul_lo_u32 v2, v1, v4
	v_add_u32_e32 v1, v2, v1
	v_cmp_ne_u32_e32 vcc, v5, v1
	v_mov_b64_e32 v[2:3], s[10:11]
	s_and_saveexec_b64 s[8:9], vcc
	s_cbranch_execz .LBB0_109
	v_mov_b32_e32 v1, 0
	global_load_dword v2, v1, s[10:11] sc1
	s_mov_b64 s[16:17], 0
	s_waitcnt vmcnt(0)
	v_cmp_eq_u32_e32 vcc, v2, v4
	s_and_saveexec_b64 s[14:15], vcc
	s_cbranch_execz .LBB0_108
	s_add_u32 s12, s90, 0x200
	s_addc_u32 s13, s91, 0
	s_mov_b32 s3, 1
	s_branch .LBB0_101

; __device__ __forceinline__ unsigned xb_add(unsigned* p, unsigned v) { return __hip_atomic_fetch_add(p, v, __ATOMIC_RELAXED, __HIP_MEMORY_SCOPE_AGENT); }
; __device__ __forceinline__ void xcd_barrier(const XcdBarrier& b) {
;     ...
;             __builtin_amdgcn_fence(__ATOMIC_ACQUIRE, "agent");
;             xb_add(&bar[XB_XGEN(b.x)], 1u);
;             asm volatile("s_waitcnt vmcnt(0)" ::: "memory");
.LBB0_111:
	s_or_b64 exec, exec, s[8:9]
	s_mov_b64 s[8:9], exec
	v_mbcnt_lo_u32_b32 v1, s8, 0
	v_mbcnt_hi_u32_b32 v1, s9, v1
	v_cmp_eq_u32_e32 vcc, 0, v1
	s_waitcnt vmcnt(0)
	s_and_saveexec_b64 s[10:11], vcc
	s_cbranch_execz .LBB0_113
	s_bcnt1_i32_b64 s3, s[8:9]
	v_mov_b32_e32 v1, 0x2000
	v_mov_b32_e32 v2, s3
	global_atomic_add v1, v2, s[6:7] offset:1024

; __device__ __forceinline__ unsigned xb_ld(unsigned* p)              { return __hip_atomic_load(p, __ATOMIC_RELAXED, __HIP_MEMORY_SCOPE_AGENT); }
; __device__ __forceinline__ unsigned xb_add(unsigned* p, unsigned v) { return __hip_atomic_fetch_add(p, v, __ATOMIC_RELAXED, __HIP_MEMORY_SCOPE_AGENT); }
; #define XB_SPIN(cond, bar) do { unsigned _sp = 0; while (cond) { __builtin_amdgcn_s_sleep(1); \
;     if ((++_sp & 255u) == 0u) { if (xb_ld(&(bar)[XB_TMO])) break; if (_sp > XB_SPIN_CAP) { atomicAdd(&(bar)[XB_TMO], 1u); break; } } } } while (0)
; __device__ __forceinline__ void xcd_barrier(const XcdBarrier& b) {
;     ...
;         unsigned nloc = b.st[0], nx = b.st[1];
;         if (nloc == 0u) { xcd_barrier_complete(bar, b.x, nloc, nx); b.st[0] = nloc; b.st[1] = nx; }
;         const unsigned old = xb_add(&bar[XB_XSUB(b.x)], 1u);
;         const unsigned gen = old / nloc;
;         if (old + 1u == (gen + 1u) * nloc) {
;             __builtin_amdgcn_fence(__ATOMIC_RELEASE, "agent");
;             asm volatile("s_waitcnt vmcnt(0)" ::: "memory");
;             const unsigned og = xb_add(&bar[XB_TOP], 1u);
;             const unsigned tg = og / nx;
;             if (og + 1u == (tg + 1u) * nx) xb_add(&bar[XB_TOPGEN], 1u);
;             else XB_SPIN(xb_ld(&bar[XB_TOPGEN]) == tg, bar);
;             __builtin_amdgcn_fence(__ATOMIC_ACQUIRE, "agent");
;             xb_add(&bar[XB_XGEN(b.x)], 1u);
;             asm volatile("s_waitcnt vmcnt(0)" ::: "memory");
;         } else {
;             XB_SPIN(xb_ld(&bar[XB_XGEN(b.x)]) == gen, bar);
.LBB0_141:
	s_or_b64 exec, exec, s[6:7]
	v_cvt_f32_u32_e32 v5, v3
	s_waitcnt vmcnt(0)
	v_readfirstlane_b32 s4, v4
	v_sub_u32_e32 v4, 0, v3
	v_rcp_iflag_f32_e32 v5, v5
	v_add_u32_e32 v6, s4, v2
	v_mul_f32_e32 v5, 0x4f7ffffe, v5
	v_cvt_u32_f32_e32 v5, v5
	v_mul_lo_u32 v2, v4, v5
	v_mul_hi_u32 v2, v5, v2
	v_add_u32_e32 v2, v5, v2
	v_mul_hi_u32 v2, v6, v2
	v_mul_lo_u32 v4, v2, v3
	v_sub_u32_e32 v4, v6, v4
	v_add_u32_e32 v5, 1, v2
	v_cmp_ge_u32_e32 vcc, v4, v3
	s_nop 1
	v_cndmask_b32_e32 v2, v2, v5, vcc
	v_sub_u32_e32 v5, v4, v3
	v_cndmask_b32_e32 v4, v4, v5, vcc
	v_add_u32_e32 v5, 1, v2
	v_cmp_ge_u32_e32 vcc, v4, v3
	v_add_u32_e32 v4, 1, v6
	s_nop 0
	v_cndmask_b32_e32 v2, v2, v5, vcc
	v_mul_lo_u32 v5, v3, v2
	v_add_u32_e32 v3, v5, v3
	v_cmp_ne_u32_e32 vcc, v4, v3
	s_and_saveexec_b64 s[4:5], vcc
	s_xor_b64 s[4:5], exec, s[4:5]
	s_cbranch_execz .LBB0_155
	s_waitcnt lgkmcnt(0)
	buffer_inv sc1
	v_mov_b32_e32 v1, 0x2000
	global_load_dword v1, v1, s[2:3] offset:1024 sc1
	s_add_u32 s8, s2, 0x2400
	s_addc_u32 s9, s3, 0
	s_waitcnt vmcnt(0)
	v_cmp_eq_u32_e32 vcc, v1, v2
	s_and_saveexec_b64 s[6:7], vcc
	s_cbranch_execz .LBB0_154
	s_mov_b32 s22, 1
	s_mov_b64 s[12:13], 0
	v_mov_b32_e32 v1, 0
	s_branch .LBB0_145

; __device__ __forceinline__ unsigned xb_ld(unsigned* p)              { return __hip_atomic_load(p, __ATOMIC_RELAXED, __HIP_MEMORY_SCOPE_AGENT); }
; #define XB_SPIN(cond, bar) do { unsigned _sp = 0; while (cond) { __builtin_amdgcn_s_sleep(1); \
;     if ((++_sp & 255u) == 0u) { if (xb_ld(&(bar)[XB_TMO])) break; if (_sp > XB_SPIN_CAP) { atomicAdd(&(bar)[XB_TMO], 1u); break; } } } } while (0)
; __device__ __forceinline__ void xcd_barrier(const XcdBarrier& b) {
;     ...
;             XB_SPIN(xb_ld(&bar[XB_XGEN(b.x)]) == gen, bar);
;             __builtin_amdgcn_fence(__ATOMIC_ACQUIRE, "agent");
;             asm volatile("s_waitcnt vmcnt(0)" ::: "memory");
.LBB0_154:
	s_or_b64 exec, exec, s[6:7]
	s_waitcnt vmcnt(0)
	s_waitcnt vmcnt(0)

; __device__ __forceinline__ unsigned xb_ld(unsigned* p)              { return __hip_atomic_load(p, __ATOMIC_RELAXED, __HIP_MEMORY_SCOPE_AGENT); }
; __device__ __forceinline__ unsigned xb_add(unsigned* p, unsigned v) { return __hip_atomic_fetch_add(p, v, __ATOMIC_RELAXED, __HIP_MEMORY_SCOPE_AGENT); }
; #define XB_SPIN(cond, bar) do { unsigned _sp = 0; while (cond) { __builtin_amdgcn_s_sleep(1); \
;     if ((++_sp & 255u) == 0u) { if (xb_ld(&(bar)[XB_TMO])) break; if (_sp > XB_SPIN_CAP) { atomicAdd(&(bar)[XB_TMO], 1u); break; } } } } while (0)
; __device__ __forceinline__ void xcd_barrier(const XcdBarrier& b) {
;     ...
;             const unsigned og = xb_add(&bar[XB_TOP], 1u);
;             const unsigned tg = og / nx;
;             if (og + 1u == (tg + 1u) * nx) xb_add(&bar[XB_TOPGEN], 1u);
;             else XB_SPIN(xb_ld(&bar[XB_TOPGEN]) == tg, bar);
.LBB0_158:
	s_or_b64 exec, exec, s[6:7]
	buffer_inv sc1
	v_cvt_f32_u32_e32 v4, v1
	s_waitcnt vmcnt(0)
	v_readfirstlane_b32 s4, v3
	s_add_u32 s6, s90, 0x3500
	s_addc_u32 s7, s91, 0
	v_rcp_iflag_f32_e32 v4, v4
	v_add_u32_e32 v2, s4, v2
	v_add_u32_e32 v5, 1, v2
	s_mov_b64 s[8:9], -1
	v_mul_f32_e32 v3, 0x4f7ffffe, v4
	v_cvt_u32_f32_e32 v3, v3
	v_sub_u32_e32 v4, 0, v1
	v_mul_lo_u32 v4, v4, v3
	v_mul_hi_u32 v4, v3, v4
	v_add_u32_e32 v3, v3, v4
	v_mul_hi_u32 v3, v2, v3
	v_mul_lo_u32 v4, v3, v1
	v_sub_u32_e32 v2, v2, v4
	v_add_u32_e32 v6, 1, v3
	v_cmp_ge_u32_e32 vcc, v2, v1
	v_sub_u32_e32 v4, v2, v1
	s_nop 0
	v_cndmask_b32_e32 v3, v3, v6, vcc
	v_cndmask_b32_e32 v2, v2, v4, vcc
	v_add_u32_e32 v4, 1, v3
	v_cmp_ge_u32_e32 vcc, v2, v1
	s_nop 1
	v_cndmask_b32_e32 v4, v3, v4, vcc
	v_mul_lo_u32 v2, v1, v4
	v_add_u32_e32 v1, v2, v1
	v_cmp_ne_u32_e32 vcc, v5, v1
	v_mov_b64_e32 v[2:3], s[6:7]
	s_and_saveexec_b64 s[4:5], vcc
	s_cbranch_execz .LBB0_170
	v_mov_b32_e32 v1, 0
	global_load_dword v2, v1, s[6:7] sc1
	s_mov_b64 s[14:15], 0
	s_waitcnt vmcnt(0)
	v_cmp_eq_u32_e32 vcc, v2, v4
	s_and_saveexec_b64 s[12:13], vcc
	s_cbranch_execz .LBB0_169
	s_add_u32 s8, s90, 0x200
	s_addc_u32 s9, s91, 0
	s_mov_b32 s24, 1
	s_branch .LBB0_162

; __device__ __forceinline__ unsigned xb_add(unsigned* p, unsigned v) { return __hip_atomic_fetch_add(p, v, __ATOMIC_RELAXED, __HIP_MEMORY_SCOPE_AGENT); }
; __device__ __forceinline__ void xcd_barrier(const XcdBarrier& b) {
;     ...
;             __builtin_amdgcn_fence(__ATOMIC_ACQUIRE, "agent");
;             xb_add(&bar[XB_XGEN(b.x)], 1u);
;             asm volatile("s_waitcnt vmcnt(0)" ::: "memory");
.LBB0_172:
	s_or_b64 exec, exec, s[4:5]
	s_mov_b64 s[4:5], exec
	v_mbcnt_lo_u32_b32 v1, s4, 0
	v_mbcnt_hi_u32_b32 v1, s5, v1
	v_cmp_eq_u32_e32 vcc, 0, v1
	s_waitcnt vmcnt(0)
	s_and_saveexec_b64 s[6:7], vcc
	s_cbranch_execz .LBB0_174
	s_bcnt1_i32_b64 s4, s[4:5]
	v_mov_b32_e32 v1, 0x2000
	v_mov_b32_e32 v2, s4
	global_atomic_add v1, v2, s[2:3] offset:1024

; __device__ __forceinline__ unsigned xb_ld(unsigned* p)              { return __hip_atomic_load(p, __ATOMIC_RELAXED, __HIP_MEMORY_SCOPE_AGENT); }
; __device__ __forceinline__ unsigned xb_add(unsigned* p, unsigned v) { return __hip_atomic_fetch_add(p, v, __ATOMIC_RELAXED, __HIP_MEMORY_SCOPE_AGENT); }
; #define XB_SPIN(cond, bar) do { unsigned _sp = 0; while (cond) { __builtin_amdgcn_s_sleep(1); \
;     if ((++_sp & 255u) == 0u) { if (xb_ld(&(bar)[XB_TMO])) break; if (_sp > XB_SPIN_CAP) { atomicAdd(&(bar)[XB_TMO], 1u); break; } } } } while (0)
; __device__ __forceinline__ void xcd_barrier(const XcdBarrier& b) {
;     ...
;         unsigned nloc = b.st[0], nx = b.st[1];
;         if (nloc == 0u) { xcd_barrier_complete(bar, b.x, nloc, nx); b.st[0] = nloc; b.st[1] = nx; }
;         const unsigned old = xb_add(&bar[XB_XSUB(b.x)], 1u);
;         const unsigned gen = old / nloc;
;         if (old + 1u == (gen + 1u) * nloc) {
;             __builtin_amdgcn_fence(__ATOMIC_RELEASE, "agent");
;             asm volatile("s_waitcnt vmcnt(0)" ::: "memory");
;             const unsigned og = xb_add(&bar[XB_TOP], 1u);
;             const unsigned tg = og / nx;
;             if (og + 1u == (tg + 1u) * nx) xb_add(&bar[XB_TOPGEN], 1u);
;             else XB_SPIN(xb_ld(&bar[XB_TOPGEN]) == tg, bar);
;             __builtin_amdgcn_fence(__ATOMIC_ACQUIRE, "agent");
;             xb_add(&bar[XB_XGEN(b.x)], 1u);
;             asm volatile("s_waitcnt vmcnt(0)" ::: "memory");
;         } else {
;             XB_SPIN(xb_ld(&bar[XB_XGEN(b.x)]) == gen, bar);
.LBB0_241:
	s_or_b64 exec, exec, s[14:15]
	v_cvt_f32_u32_e32 v5, v3
	s_waitcnt vmcnt(0)
	v_readfirstlane_b32 s12, v4
	v_sub_u32_e32 v4, 0, v3
	v_rcp_iflag_f32_e32 v5, v5
	v_add_u32_e32 v6, s12, v2
	v_mul_f32_e32 v5, 0x4f7ffffe, v5
	v_cvt_u32_f32_e32 v5, v5
	v_mul_lo_u32 v2, v4, v5
	v_mul_hi_u32 v2, v5, v2
	v_add_u32_e32 v2, v5, v2
	v_mul_hi_u32 v2, v6, v2
	v_mul_lo_u32 v4, v2, v3
	v_sub_u32_e32 v4, v6, v4
	v_add_u32_e32 v5, 1, v2
	v_cmp_ge_u32_e32 vcc, v4, v3
	s_nop 1
	v_cndmask_b32_e32 v2, v2, v5, vcc
	v_sub_u32_e32 v5, v4, v3
	v_cndmask_b32_e32 v4, v4, v5, vcc
	v_add_u32_e32 v5, 1, v2
	v_cmp_ge_u32_e32 vcc, v4, v3
	v_add_u32_e32 v4, 1, v6
	s_nop 0
	v_cndmask_b32_e32 v2, v2, v5, vcc
	v_mul_lo_u32 v5, v3, v2
	v_add_u32_e32 v3, v5, v3
	v_cmp_ne_u32_e32 vcc, v4, v3
	s_and_saveexec_b64 s[12:13], vcc
	s_xor_b64 s[12:13], exec, s[12:13]
	s_cbranch_execz .LBB0_255
	s_waitcnt lgkmcnt(0)
	buffer_inv sc1
	v_mov_b32_e32 v1, 0x2000
	global_load_dword v1, v1, s[4:5] offset:1024 sc1
	s_add_u32 s16, s4, 0x2400
	s_addc_u32 s17, s5, 0
	s_waitcnt vmcnt(0)
	v_cmp_eq_u32_e32 vcc, v1, v2
	s_and_saveexec_b64 s[14:15], vcc
	s_cbranch_execz .LBB0_254
	s_mov_b32 s28, 1
	s_mov_b64 s[18:19], 0
	v_mov_b32_e32 v1, 0
	s_branch .LBB0_245

; __device__ __forceinline__ unsigned xb_ld(unsigned* p)              { return __hip_atomic_load(p, __ATOMIC_RELAXED, __HIP_MEMORY_SCOPE_AGENT); }
; #define XB_SPIN(cond, bar) do { unsigned _sp = 0; while (cond) { __builtin_amdgcn_s_sleep(1); \
;     if ((++_sp & 255u) == 0u) { if (xb_ld(&(bar)[XB_TMO])) break; if (_sp > XB_SPIN_CAP) { atomicAdd(&(bar)[XB_TMO], 1u); break; } } } } while (0)
; __device__ __forceinline__ void xcd_barrier(const XcdBarrier& b) {
;     ...
;             XB_SPIN(xb_ld(&bar[XB_XGEN(b.x)]) == gen, bar);
;             __builtin_amdgcn_fence(__ATOMIC_ACQUIRE, "agent");
;             asm volatile("s_waitcnt vmcnt(0)" ::: "memory");
.LBB0_254:
	s_or_b64 exec, exec, s[14:15]
	s_waitcnt vmcnt(0)
	s_waitcnt vmcnt(0)

; __device__ __forceinline__ unsigned xb_ld(unsigned* p)              { return __hip_atomic_load(p, __ATOMIC_RELAXED, __HIP_MEMORY_SCOPE_AGENT); }
; __device__ __forceinline__ unsigned xb_add(unsigned* p, unsigned v) { return __hip_atomic_fetch_add(p, v, __ATOMIC_RELAXED, __HIP_MEMORY_SCOPE_AGENT); }
; #define XB_SPIN(cond, bar) do { unsigned _sp = 0; while (cond) { __builtin_amdgcn_s_sleep(1); \
;     if ((++_sp & 255u) == 0u) { if (xb_ld(&(bar)[XB_TMO])) break; if (_sp > XB_SPIN_CAP) { atomicAdd(&(bar)[XB_TMO], 1u); break; } } } } while (0)
; __device__ __forceinline__ void xcd_barrier(const XcdBarrier& b) {
;     ...
;             const unsigned og = xb_add(&bar[XB_TOP], 1u);
;             const unsigned tg = og / nx;
;             if (og + 1u == (tg + 1u) * nx) xb_add(&bar[XB_TOPGEN], 1u);
;             else XB_SPIN(xb_ld(&bar[XB_TOPGEN]) == tg, bar);
.LBB0_258:
	s_or_b64 exec, exec, s[14:15]
	buffer_inv sc1
	v_cvt_f32_u32_e32 v4, v1
	s_waitcnt vmcnt(0)
	v_readfirstlane_b32 s12, v3
	s_add_u32 s14, s90, 0x3500
	s_addc_u32 s15, s91, 0
	v_rcp_iflag_f32_e32 v4, v4
	v_add_u32_e32 v2, s12, v2
	v_add_u32_e32 v5, 1, v2
	s_mov_b64 s[16:17], -1
	v_mul_f32_e32 v3, 0x4f7ffffe, v4
	v_cvt_u32_f32_e32 v3, v3
	v_sub_u32_e32 v4, 0, v1
	v_mul_lo_u32 v4, v4, v3
	v_mul_hi_u32 v4, v3, v4
	v_add_u32_e32 v3, v3, v4
	v_mul_hi_u32 v3, v2, v3
	v_mul_lo_u32 v4, v3, v1
	v_sub_u32_e32 v2, v2, v4
	v_add_u32_e32 v6, 1, v3
	v_cmp_ge_u32_e32 vcc, v2, v1
	v_sub_u32_e32 v4, v2, v1
	s_nop 0
	v_cndmask_b32_e32 v3, v3, v6, vcc
	v_cndmask_b32_e32 v2, v2, v4, vcc
	v_add_u32_e32 v4, 1, v3
	v_cmp_ge_u32_e32 vcc, v2, v1
	s_nop 1
	v_cndmask_b32_e32 v4, v3, v4, vcc
	v_mul_lo_u32 v2, v1, v4
	v_add_u32_e32 v1, v2, v1
	v_cmp_ne_u32_e32 vcc, v5, v1
	v_mov_b64_e32 v[2:3], s[14:15]
	s_and_saveexec_b64 s[12:13], vcc
	s_cbranch_execz .LBB0_270
	v_mov_b32_e32 v1, 0
	global_load_dword v2, v1, s[14:15] sc1
	s_mov_b64 s[20:21], 0
	s_waitcnt vmcnt(0)
	v_cmp_eq_u32_e32 vcc, v2, v4
	s_and_saveexec_b64 s[18:19], vcc
	s_cbranch_execz .LBB0_269
	s_add_u32 s16, s90, 0x200
	s_addc_u32 s17, s91, 0
	s_mov_b32 s30, 1
	s_branch .LBB0_262

; __device__ __forceinline__ unsigned xb_add(unsigned* p, unsigned v) { return __hip_atomic_fetch_add(p, v, __ATOMIC_RELAXED, __HIP_MEMORY_SCOPE_AGENT); }
; __device__ __forceinline__ void xcd_barrier(const XcdBarrier& b) {
;     ...
;             __builtin_amdgcn_fence(__ATOMIC_ACQUIRE, "agent");
;             xb_add(&bar[XB_XGEN(b.x)], 1u);
;             asm volatile("s_waitcnt vmcnt(0)" ::: "memory");
.LBB0_272:
	s_or_b64 exec, exec, s[12:13]
	s_mov_b64 s[12:13], exec
	v_mbcnt_lo_u32_b32 v1, s12, 0
	v_mbcnt_hi_u32_b32 v1, s13, v1
	v_cmp_eq_u32_e32 vcc, 0, v1
	s_waitcnt vmcnt(0)
	s_and_saveexec_b64 s[14:15], vcc
	s_cbranch_execz .LBB0_274
	s_bcnt1_i32_b64 s12, s[12:13]
	v_mov_b32_e32 v1, 0x2000
	v_mov_b32_e32 v2, s12
	global_atomic_add v1, v2, s[4:5] offset:1024

; __device__ __forceinline__ unsigned xb_ld(unsigned* p)              { return __hip_atomic_load(p, __ATOMIC_RELAXED, __HIP_MEMORY_SCOPE_AGENT); }
; __device__ __forceinline__ unsigned xb_add(unsigned* p, unsigned v) { return __hip_atomic_fetch_add(p, v, __ATOMIC_RELAXED, __HIP_MEMORY_SCOPE_AGENT); }
; #define XB_SPIN(cond, bar) do { unsigned _sp = 0; while (cond) { __builtin_amdgcn_s_sleep(1); \
;     if ((++_sp & 255u) == 0u) { if (xb_ld(&(bar)[XB_TMO])) break; if (_sp > XB_SPIN_CAP) { atomicAdd(&(bar)[XB_TMO], 1u); break; } } } } while (0)
; __device__ __forceinline__ void xcd_barrier(const XcdBarrier& b) {
;     ...
;         unsigned nloc = b.st[0], nx = b.st[1];
;         if (nloc == 0u) { xcd_barrier_complete(bar, b.x, nloc, nx); b.st[0] = nloc; b.st[1] = nx; }
;         const unsigned old = xb_add(&bar[XB_XSUB(b.x)], 1u);
;         const unsigned gen = old / nloc;
;         if (old + 1u == (gen + 1u) * nloc) {
;             __builtin_amdgcn_fence(__ATOMIC_RELEASE, "agent");
;             asm volatile("s_waitcnt vmcnt(0)" ::: "memory");
;             const unsigned og = xb_add(&bar[XB_TOP], 1u);
;             const unsigned tg = og / nx;
;             if (og + 1u == (tg + 1u) * nx) xb_add(&bar[XB_TOPGEN], 1u);
;             else XB_SPIN(xb_ld(&bar[XB_TOPGEN]) == tg, bar);
;             __builtin_amdgcn_fence(__ATOMIC_ACQUIRE, "agent");
;             xb_add(&bar[XB_XGEN(b.x)], 1u);
;             asm volatile("s_waitcnt vmcnt(0)" ::: "memory");
;         } else {
;             XB_SPIN(xb_ld(&bar[XB_XGEN(b.x)]) == gen, bar);
.LBB0_661:
	s_or_b64 exec, exec, s[6:7]
	v_cvt_f32_u32_e32 v5, v3
	s_waitcnt vmcnt(0)
	v_readfirstlane_b32 s4, v4
	v_sub_u32_e32 v4, 0, v3
	v_rcp_iflag_f32_e32 v5, v5
	v_add_u32_e32 v6, s4, v2
	v_mul_f32_e32 v5, 0x4f7ffffe, v5
	v_cvt_u32_f32_e32 v5, v5
	v_mul_lo_u32 v2, v4, v5
	v_mul_hi_u32 v2, v5, v2
	v_add_u32_e32 v2, v5, v2
	v_mul_hi_u32 v2, v6, v2
	v_mul_lo_u32 v4, v2, v3
	v_sub_u32_e32 v4, v6, v4
	v_add_u32_e32 v5, 1, v2
	v_cmp_ge_u32_e32 vcc, v4, v3
	s_nop 1
	v_cndmask_b32_e32 v2, v2, v5, vcc
	v_sub_u32_e32 v5, v4, v3
	v_cndmask_b32_e32 v4, v4, v5, vcc
	v_add_u32_e32 v5, 1, v2
	v_cmp_ge_u32_e32 vcc, v4, v3
	v_add_u32_e32 v4, 1, v6
	s_nop 0
	v_cndmask_b32_e32 v2, v2, v5, vcc
	v_mul_lo_u32 v5, v3, v2
	v_add_u32_e32 v3, v5, v3
	v_cmp_ne_u32_e32 vcc, v4, v3
	s_and_saveexec_b64 s[4:5], vcc
	s_xor_b64 s[4:5], exec, s[4:5]
	s_cbranch_execz .LBB0_675
	s_waitcnt lgkmcnt(0)
	buffer_inv sc1
	v_mov_b32_e32 v1, 0x2000
	global_load_dword v1, v1, s[2:3] offset:1024 sc1
	s_add_u32 s8, s2, 0x2400
	s_addc_u32 s9, s3, 0
	s_waitcnt vmcnt(0)
	v_cmp_eq_u32_e32 vcc, v1, v2
	s_and_saveexec_b64 s[6:7], vcc
	s_cbranch_execz .LBB0_674
	s_mov_b32 s20, 1
	s_mov_b64 s[10:11], 0
	v_mov_b32_e32 v1, 0
	s_branch .LBB0_665

; __device__ __forceinline__ unsigned xb_ld(unsigned* p)              { return __hip_atomic_load(p, __ATOMIC_RELAXED, __HIP_MEMORY_SCOPE_AGENT); }
; __device__ __forceinline__ unsigned xb_add(unsigned* p, unsigned v) { return __hip_atomic_fetch_add(p, v, __ATOMIC_RELAXED, __HIP_MEMORY_SCOPE_AGENT); }
; #define XB_SPIN(cond, bar) do { unsigned _sp = 0; while (cond) { __builtin_amdgcn_s_sleep(1); \
;     if ((++_sp & 255u) == 0u) { if (xb_ld(&(bar)[XB_TMO])) break; if (_sp > XB_SPIN_CAP) { atomicAdd(&(bar)[XB_TMO], 1u); break; } } } } while (0)
; __device__ __forceinline__ void xcd_barrier(const XcdBarrier& b) {
;     ...
;             const unsigned og = xb_add(&bar[XB_TOP], 1u);
;             const unsigned tg = og / nx;
;             if (og + 1u == (tg + 1u) * nx) xb_add(&bar[XB_TOPGEN], 1u);
;             else XB_SPIN(xb_ld(&bar[XB_TOPGEN]) == tg, bar);
.LBB0_678:
	s_or_b64 exec, exec, s[6:7]
	buffer_inv sc1
	v_cvt_f32_u32_e32 v4, v1
	s_waitcnt vmcnt(0)
	v_readfirstlane_b32 s4, v3
	s_add_u32 s6, s90, 0x3500
	s_addc_u32 s7, s91, 0
	v_rcp_iflag_f32_e32 v4, v4
	v_add_u32_e32 v2, s4, v2
	v_add_u32_e32 v5, 1, v2
	s_mov_b64 s[8:9], -1
	v_mul_f32_e32 v3, 0x4f7ffffe, v4
	v_cvt_u32_f32_e32 v3, v3
	v_sub_u32_e32 v4, 0, v1
	v_mul_lo_u32 v4, v4, v3
	v_mul_hi_u32 v4, v3, v4
	v_add_u32_e32 v3, v3, v4
	v_mul_hi_u32 v3, v2, v3
	v_mul_lo_u32 v4, v3, v1
	v_sub_u32_e32 v2, v2, v4
	v_add_u32_e32 v6, 1, v3
	v_cmp_ge_u32_e32 vcc, v2, v1
	v_sub_u32_e32 v4, v2, v1
	s_nop 0
	v_cndmask_b32_e32 v3, v3, v6, vcc
	v_cndmask_b32_e32 v2, v2, v4, vcc
	v_add_u32_e32 v4, 1, v3
	v_cmp_ge_u32_e32 vcc, v2, v1
	s_nop 1
	v_cndmask_b32_e32 v4, v3, v4, vcc
	v_mul_lo_u32 v2, v1, v4
	v_add_u32_e32 v1, v2, v1
	v_cmp_ne_u32_e32 vcc, v5, v1
	v_mov_b64_e32 v[2:3], s[6:7]
	s_and_saveexec_b64 s[4:5], vcc
	s_cbranch_execz .LBB0_690
	v_mov_b32_e32 v1, 0
	global_load_dword v2, v1, s[6:7] sc1
	s_mov_b64 s[12:13], 0
	s_waitcnt vmcnt(0)
	v_cmp_eq_u32_e32 vcc, v2, v4
	s_and_saveexec_b64 s[10:11], vcc
	s_cbranch_execz .LBB0_689
	s_add_u32 s8, s90, 0x200
	s_addc_u32 s9, s91, 0
	s_mov_b32 s22, 1
	s_branch .LBB0_682

; __device__ __forceinline__ unsigned xb_ld(unsigned* p)              { return __hip_atomic_load(p, __ATOMIC_RELAXED, __HIP_MEMORY_SCOPE_AGENT); }
; __device__ __forceinline__ unsigned xb_add(unsigned* p, unsigned v) { return __hip_atomic_fetch_add(p, v, __ATOMIC_RELAXED, __HIP_MEMORY_SCOPE_AGENT); }
; #define XB_SPIN(cond, bar) do { unsigned _sp = 0; while (cond) { __builtin_amdgcn_s_sleep(1); \
;     if ((++_sp & 255u) == 0u) { if (xb_ld(&(bar)[XB_TMO])) break; if (_sp > XB_SPIN_CAP) { atomicAdd(&(bar)[XB_TMO], 1u); break; } } } } while (0)
; __device__ __forceinline__ void xcd_barrier(const XcdBarrier& b) {
;     ...
;         unsigned nloc = b.st[0], nx = b.st[1];
;         if (nloc == 0u) { xcd_barrier_complete(bar, b.x, nloc, nx); b.st[0] = nloc; b.st[1] = nx; }
;         const unsigned old = xb_add(&bar[XB_XSUB(b.x)], 1u);
;         const unsigned gen = old / nloc;
;         if (old + 1u == (gen + 1u) * nloc) {
;             __builtin_amdgcn_fence(__ATOMIC_RELEASE, "agent");
;             asm volatile("s_waitcnt vmcnt(0)" ::: "memory");
;             const unsigned og = xb_add(&bar[XB_TOP], 1u);
;             const unsigned tg = og / nx;
;             if (og + 1u == (tg + 1u) * nx) xb_add(&bar[XB_TOPGEN], 1u);
;             else XB_SPIN(xb_ld(&bar[XB_TOPGEN]) == tg, bar);
;             __builtin_amdgcn_fence(__ATOMIC_ACQUIRE, "agent");
;             xb_add(&bar[XB_XGEN(b.x)], 1u);
;             asm volatile("s_waitcnt vmcnt(0)" ::: "memory");
;         } else {
;             XB_SPIN(xb_ld(&bar[XB_XGEN(b.x)]) == gen, bar);
.LBB0_1212:
	s_or_b64 exec, exec, s[8:9]
	v_cvt_f32_u32_e32 v5, v3
	s_waitcnt vmcnt(0)
	v_readfirstlane_b32 s6, v4
	v_sub_u32_e32 v4, 0, v3
	v_rcp_iflag_f32_e32 v5, v5
	v_add_u32_e32 v6, s6, v2
	v_mul_f32_e32 v5, 0x4f7ffffe, v5
	v_cvt_u32_f32_e32 v5, v5
	v_mul_lo_u32 v2, v4, v5
	v_mul_hi_u32 v2, v5, v2
	v_add_u32_e32 v2, v5, v2
	v_mul_hi_u32 v2, v6, v2
	v_mul_lo_u32 v4, v2, v3
	v_sub_u32_e32 v4, v6, v4
	v_add_u32_e32 v5, 1, v2
	v_cmp_ge_u32_e32 vcc, v4, v3
	s_nop 1
	v_cndmask_b32_e32 v2, v2, v5, vcc
	v_sub_u32_e32 v5, v4, v3
	v_cndmask_b32_e32 v4, v4, v5, vcc
	v_add_u32_e32 v5, 1, v2
	v_cmp_ge_u32_e32 vcc, v4, v3
	v_add_u32_e32 v4, 1, v6
	s_nop 0
	v_cndmask_b32_e32 v2, v2, v5, vcc
	v_mul_lo_u32 v5, v3, v2
	v_add_u32_e32 v3, v5, v3
	v_cmp_ne_u32_e32 vcc, v4, v3
	s_and_saveexec_b64 s[6:7], vcc
	s_xor_b64 s[6:7], exec, s[6:7]
	s_cbranch_execz .LBB0_1226
	s_waitcnt lgkmcnt(0)
	buffer_inv sc1
	v_mov_b32_e32 v1, 0x2000
	global_load_dword v1, v1, s[2:3] offset:1024 sc1
	s_add_u32 s10, s2, 0x2400
	s_addc_u32 s11, s3, 0
	s_waitcnt vmcnt(0)
	v_cmp_eq_u32_e32 vcc, v1, v2
	s_and_saveexec_b64 s[8:9], vcc
	s_cbranch_execz .LBB0_1225
	s_mov_b32 s22, 1
	s_mov_b64 s[12:13], 0
	v_mov_b32_e32 v1, 0
	s_branch .LBB0_1216

; __device__ __forceinline__ unsigned xb_ld(unsigned* p)              { return __hip_atomic_load(p, __ATOMIC_RELAXED, __HIP_MEMORY_SCOPE_AGENT); }
; #define XB_SPIN(cond, bar) do { unsigned _sp = 0; while (cond) { __builtin_amdgcn_s_sleep(1); \
;     if ((++_sp & 255u) == 0u) { if (xb_ld(&(bar)[XB_TMO])) break; if (_sp > XB_SPIN_CAP) { atomicAdd(&(bar)[XB_TMO], 1u); break; } } } } while (0)
; __device__ __forceinline__ void xcd_barrier(const XcdBarrier& b) {
;     ...
;             XB_SPIN(xb_ld(&bar[XB_XGEN(b.x)]) == gen, bar);
;             __builtin_amdgcn_fence(__ATOMIC_ACQUIRE, "agent");
;             asm volatile("s_waitcnt vmcnt(0)" ::: "memory");
.LBB0_1225:
	s_or_b64 exec, exec, s[8:9]
	s_waitcnt vmcnt(0)
	s_waitcnt vmcnt(0)

; __device__ __forceinline__ unsigned xb_ld(unsigned* p)              { return __hip_atomic_load(p, __ATOMIC_RELAXED, __HIP_MEMORY_SCOPE_AGENT); }
; __device__ __forceinline__ unsigned xb_add(unsigned* p, unsigned v) { return __hip_atomic_fetch_add(p, v, __ATOMIC_RELAXED, __HIP_MEMORY_SCOPE_AGENT); }
; #define XB_SPIN(cond, bar) do { unsigned _sp = 0; while (cond) { __builtin_amdgcn_s_sleep(1); \
;     if ((++_sp & 255u) == 0u) { if (xb_ld(&(bar)[XB_TMO])) break; if (_sp > XB_SPIN_CAP) { atomicAdd(&(bar)[XB_TMO], 1u); break; } } } } while (0)
; __device__ __forceinline__ void xcd_barrier(const XcdBarrier& b) {
;     ...
;             const unsigned og = xb_add(&bar[XB_TOP], 1u);
;             const unsigned tg = og / nx;
;             if (og + 1u == (tg + 1u) * nx) xb_add(&bar[XB_TOPGEN], 1u);
;             else XB_SPIN(xb_ld(&bar[XB_TOPGEN]) == tg, bar);
.LBB0_1229:
	s_or_b64 exec, exec, s[8:9]
	buffer_inv sc1
	v_cvt_f32_u32_e32 v4, v1
	s_waitcnt vmcnt(0)
	v_readfirstlane_b32 s6, v3
	s_add_u32 s8, s90, 0x3500
	s_addc_u32 s9, s91, 0
	v_rcp_iflag_f32_e32 v4, v4
	v_add_u32_e32 v2, s6, v2
	v_add_u32_e32 v5, 1, v2
	s_mov_b64 s[10:11], -1
	v_mul_f32_e32 v3, 0x4f7ffffe, v4
	v_cvt_u32_f32_e32 v3, v3
	v_sub_u32_e32 v4, 0, v1
	v_mul_lo_u32 v4, v4, v3
	v_mul_hi_u32 v4, v3, v4
	v_add_u32_e32 v3, v3, v4
	v_mul_hi_u32 v3, v2, v3
	v_mul_lo_u32 v4, v3, v1
	v_sub_u32_e32 v2, v2, v4
	v_add_u32_e32 v6, 1, v3
	v_cmp_ge_u32_e32 vcc, v2, v1
	v_sub_u32_e32 v4, v2, v1
	s_nop 0
	v_cndmask_b32_e32 v3, v3, v6, vcc
	v_cndmask_b32_e32 v2, v2, v4, vcc
	v_add_u32_e32 v4, 1, v3
	v_cmp_ge_u32_e32 vcc, v2, v1
	s_nop 1
	v_cndmask_b32_e32 v4, v3, v4, vcc
	v_mul_lo_u32 v2, v1, v4
	v_add_u32_e32 v1, v2, v1
	v_cmp_ne_u32_e32 vcc, v5, v1
	v_mov_b64_e32 v[2:3], s[8:9]
	s_and_saveexec_b64 s[6:7], vcc
	s_cbranch_execz .LBB0_1241
	v_mov_b32_e32 v1, 0
	global_load_dword v2, v1, s[8:9] sc1
	s_mov_b64 s[14:15], 0
	s_waitcnt vmcnt(0)
	v_cmp_eq_u32_e32 vcc, v2, v4
	s_and_saveexec_b64 s[12:13], vcc
	s_cbranch_execz .LBB0_1240
	s_add_u32 s10, s90, 0x200
	s_addc_u32 s11, s91, 0
	s_mov_b32 s24, 1
	s_branch .LBB0_1233

; __device__ __forceinline__ unsigned xb_add(unsigned* p, unsigned v) { return __hip_atomic_fetch_add(p, v, __ATOMIC_RELAXED, __HIP_MEMORY_SCOPE_AGENT); }
; __device__ __forceinline__ void xcd_barrier(const XcdBarrier& b) {
;     ...
;             __builtin_amdgcn_fence(__ATOMIC_ACQUIRE, "agent");
;             xb_add(&bar[XB_XGEN(b.x)], 1u);
;             asm volatile("s_waitcnt vmcnt(0)" ::: "memory");
.LBB0_1243:
	s_or_b64 exec, exec, s[6:7]
	s_mov_b64 s[6:7], exec
	v_mbcnt_lo_u32_b32 v1, s6, 0
	v_mbcnt_hi_u32_b32 v1, s7, v1
	v_cmp_eq_u32_e32 vcc, 0, v1
	s_waitcnt vmcnt(0)
	s_and_saveexec_b64 s[8:9], vcc
	s_cbranch_execz .LBB0_1245
	s_bcnt1_i32_b64 s6, s[6:7]
	v_mov_b32_e32 v1, 0x2000
	v_mov_b32_e32 v2, s6
	global_atomic_add v1, v2, s[2:3] offset:1024

; __device__ __forceinline__ unsigned xb_ld(unsigned* p)              { return __hip_atomic_load(p, __ATOMIC_RELAXED, __HIP_MEMORY_SCOPE_AGENT); }
; __device__ __forceinline__ unsigned xb_add(unsigned* p, unsigned v) { return __hip_atomic_fetch_add(p, v, __ATOMIC_RELAXED, __HIP_MEMORY_SCOPE_AGENT); }
; #define XB_SPIN(cond, bar) do { unsigned _sp = 0; while (cond) { __builtin_amdgcn_s_sleep(1); \
;     if ((++_sp & 255u) == 0u) { if (xb_ld(&(bar)[XB_TMO])) break; if (_sp > XB_SPIN_CAP) { atomicAdd(&(bar)[XB_TMO], 1u); break; } } } } while (0)
; __device__ __forceinline__ void xcd_barrier(const XcdBarrier& b) {
;     ...
;             const unsigned og = xb_add(&bar[XB_TOP], 1u);
;             const unsigned tg = og / nx;
;             if (og + 1u == (tg + 1u) * nx) xb_add(&bar[XB_TOPGEN], 1u);
;             else XB_SPIN(xb_ld(&bar[XB_TOPGEN]) == tg, bar);
.LBB0_1453:
	s_or_b64 exec, exec, s[8:9]
	buffer_inv sc1
	v_cvt_f32_u32_e32 v4, v1
	s_waitcnt vmcnt(0)
	v_readfirstlane_b32 s6, v3
	s_add_u32 s8, s90, 0x3500
	s_addc_u32 s9, s91, 0
	v_rcp_iflag_f32_e32 v4, v4
	v_add_u32_e32 v2, s6, v2
	v_add_u32_e32 v5, 1, v2
	s_mov_b64 s[10:11], -1
	v_mul_f32_e32 v3, 0x4f7ffffe, v4
	v_cvt_u32_f32_e32 v3, v3
	v_sub_u32_e32 v4, 0, v1
	v_mul_lo_u32 v4, v4, v3
	v_mul_hi_u32 v4, v3, v4
	v_add_u32_e32 v3, v3, v4
	v_mul_hi_u32 v3, v2, v3
	v_mul_lo_u32 v4, v3, v1
	v_sub_u32_e32 v2, v2, v4
	v_add_u32_e32 v6, 1, v3
	v_cmp_ge_u32_e32 vcc, v2, v1
	v_sub_u32_e32 v4, v2, v1
	s_nop 0
	v_cndmask_b32_e32 v3, v3, v6, vcc
	v_cndmask_b32_e32 v2, v2, v4, vcc
	v_add_u32_e32 v4, 1, v3
	v_cmp_ge_u32_e32 vcc, v2, v1
	s_nop 1
	v_cndmask_b32_e32 v4, v3, v4, vcc
	v_mul_lo_u32 v2, v1, v4
	v_add_u32_e32 v1, v2, v1
	v_cmp_ne_u32_e32 vcc, v5, v1
	v_mov_b64_e32 v[2:3], s[8:9]
	s_and_saveexec_b64 s[6:7], vcc
	s_cbranch_execz .LBB0_1465
	v_mov_b32_e32 v1, 0
	global_load_dword v2, v1, s[8:9] sc1
	s_mov_b64 s[24:25], 0
	s_waitcnt vmcnt(0)
	v_cmp_eq_u32_e32 vcc, v2, v4
	s_and_saveexec_b64 s[12:13], vcc
	s_cbranch_execz .LBB0_1464
	s_add_u32 s10, s90, 0x200
	s_addc_u32 s11, s91, 0
	s_mov_b32 s22, 1
	s_branch .LBB0_1457

; __device__ __forceinline__ unsigned xb_ld(unsigned* p)              { return __hip_atomic_load(p, __ATOMIC_RELAXED, __HIP_MEMORY_SCOPE_AGENT); }
; __device__ __forceinline__ unsigned xb_add(unsigned* p, unsigned v) { return __hip_atomic_fetch_add(p, v, __ATOMIC_RELAXED, __HIP_MEMORY_SCOPE_AGENT); }
; #define XB_SPIN(cond, bar) do { unsigned _sp = 0; while (cond) { __builtin_amdgcn_s_sleep(1); \
;     if ((++_sp & 255u) == 0u) { if (xb_ld(&(bar)[XB_TMO])) break; if (_sp > XB_SPIN_CAP) { atomicAdd(&(bar)[XB_TMO], 1u); break; } } } } while (0)
; __device__ __forceinline__ void xcd_barrier(const XcdBarrier& b) {
;     ...
;         unsigned nloc = b.st[0], nx = b.st[1];
;         if (nloc == 0u) { xcd_barrier_complete(bar, b.x, nloc, nx); b.st[0] = nloc; b.st[1] = nx; }
;         const unsigned old = xb_add(&bar[XB_XSUB(b.x)], 1u);
;         const unsigned gen = old / nloc;
;         if (old + 1u == (gen + 1u) * nloc) {
;             __builtin_amdgcn_fence(__ATOMIC_RELEASE, "agent");
;             asm volatile("s_waitcnt vmcnt(0)" ::: "memory");
;             const unsigned og = xb_add(&bar[XB_TOP], 1u);
;             const unsigned tg = og / nx;
;             if (og + 1u == (tg + 1u) * nx) xb_add(&bar[XB_TOPGEN], 1u);
;             else XB_SPIN(xb_ld(&bar[XB_TOPGEN]) == tg, bar);
;             __builtin_amdgcn_fence(__ATOMIC_ACQUIRE, "agent");
;             xb_add(&bar[XB_XGEN(b.x)], 1u);
;             asm volatile("s_waitcnt vmcnt(0)" ::: "memory");
;         } else {
;             XB_SPIN(xb_ld(&bar[XB_XGEN(b.x)]) == gen, bar);
.LBB0_1743:
	s_or_b64 exec, exec, s[8:9]
	v_cvt_f32_u32_e32 v5, v3
	s_waitcnt vmcnt(0)
	v_readfirstlane_b32 s6, v4
	v_sub_u32_e32 v4, 0, v3
	v_rcp_iflag_f32_e32 v5, v5
	v_add_u32_e32 v6, s6, v2
	v_mul_f32_e32 v5, 0x4f7ffffe, v5
	v_cvt_u32_f32_e32 v5, v5
	v_mul_lo_u32 v2, v4, v5
	v_mul_hi_u32 v2, v5, v2
	v_add_u32_e32 v2, v5, v2
	v_mul_hi_u32 v2, v6, v2
	v_mul_lo_u32 v4, v2, v3
	v_sub_u32_e32 v4, v6, v4
	v_add_u32_e32 v5, 1, v2
	v_cmp_ge_u32_e32 vcc, v4, v3
	s_nop 1
	v_cndmask_b32_e32 v2, v2, v5, vcc
	v_sub_u32_e32 v5, v4, v3
	v_cndmask_b32_e32 v4, v4, v5, vcc
	v_add_u32_e32 v5, 1, v2
	v_cmp_ge_u32_e32 vcc, v4, v3
	v_add_u32_e32 v4, 1, v6
	s_nop 0
	v_cndmask_b32_e32 v2, v2, v5, vcc
	v_mul_lo_u32 v5, v3, v2
	v_add_u32_e32 v3, v5, v3
	v_cmp_ne_u32_e32 vcc, v4, v3
	s_and_saveexec_b64 s[6:7], vcc
	s_xor_b64 s[6:7], exec, s[6:7]
	s_cbranch_execz .LBB0_1757
	s_waitcnt lgkmcnt(0)
	buffer_inv sc1
	v_mov_b32_e32 v1, 0x2000
	global_load_dword v1, v1, s[2:3] offset:1024 sc1
	s_add_u32 s10, s2, 0x2400
	s_addc_u32 s11, s3, 0
	s_waitcnt vmcnt(0)
	v_cmp_eq_u32_e32 vcc, v1, v2
	s_and_saveexec_b64 s[8:9], vcc
	s_cbranch_execz .LBB0_1756
	s_mov_b32 s26, 1
	s_mov_b64 s[12:13], 0
	v_mov_b32_e32 v1, 0
	s_branch .LBB0_1747

; __device__ __forceinline__ unsigned xb_ld(unsigned* p)              { return __hip_atomic_load(p, __ATOMIC_RELAXED, __HIP_MEMORY_SCOPE_AGENT); }
; __device__ __forceinline__ unsigned xb_add(unsigned* p, unsigned v) { return __hip_atomic_fetch_add(p, v, __ATOMIC_RELAXED, __HIP_MEMORY_SCOPE_AGENT); }
; #define XB_SPIN(cond, bar) do { unsigned _sp = 0; while (cond) { __builtin_amdgcn_s_sleep(1); \
;     if ((++_sp & 255u) == 0u) { if (xb_ld(&(bar)[XB_TMO])) break; if (_sp > XB_SPIN_CAP) { atomicAdd(&(bar)[XB_TMO], 1u); break; } } } } while (0)
; __device__ __forceinline__ void xcd_barrier(const XcdBarrier& b) {
;     ...
;             const unsigned og = xb_add(&bar[XB_TOP], 1u);
;             const unsigned tg = og / nx;
;             if (og + 1u == (tg + 1u) * nx) xb_add(&bar[XB_TOPGEN], 1u);
;             else XB_SPIN(xb_ld(&bar[XB_TOPGEN]) == tg, bar);
.LBB0_1760:
	s_or_b64 exec, exec, s[8:9]
	buffer_inv sc1
	v_cvt_f32_u32_e32 v4, v1
	s_waitcnt vmcnt(0)
	v_readfirstlane_b32 s6, v3
	s_add_u32 s8, s90, 0x3500
	s_addc_u32 s9, s91, 0
	v_rcp_iflag_f32_e32 v4, v4
	v_add_u32_e32 v2, s6, v2
	v_add_u32_e32 v5, 1, v2
	s_mov_b64 s[10:11], -1
	v_mul_f32_e32 v3, 0x4f7ffffe, v4
	v_cvt_u32_f32_e32 v3, v3
	v_sub_u32_e32 v4, 0, v1
	v_mul_lo_u32 v4, v4, v3
	v_mul_hi_u32 v4, v3, v4
	v_add_u32_e32 v3, v3, v4
	v_mul_hi_u32 v3, v2, v3
	v_mul_lo_u32 v4, v3, v1
	v_sub_u32_e32 v2, v2, v4
	v_add_u32_e32 v6, 1, v3
	v_cmp_ge_u32_e32 vcc, v2, v1
	v_sub_u32_e32 v4, v2, v1
	s_nop 0
	v_cndmask_b32_e32 v3, v3, v6, vcc
	v_cndmask_b32_e32 v2, v2, v4, vcc
	v_add_u32_e32 v4, 1, v3
	v_cmp_ge_u32_e32 vcc, v2, v1
	s_nop 1
	v_cndmask_b32_e32 v4, v3, v4, vcc
	v_mul_lo_u32 v2, v1, v4
	v_add_u32_e32 v1, v2, v1
	v_cmp_ne_u32_e32 vcc, v5, v1
	v_mov_b64_e32 v[2:3], s[8:9]
	s_and_saveexec_b64 s[6:7], vcc
	s_cbranch_execz .LBB0_1772
	v_mov_b32_e32 v1, 0
	global_load_dword v2, v1, s[8:9] sc1
	s_mov_b64 s[14:15], 0
	s_waitcnt vmcnt(0)
	v_cmp_eq_u32_e32 vcc, v2, v4
	s_and_saveexec_b64 s[12:13], vcc
	s_cbranch_execz .LBB0_1771
	s_add_u32 s10, s90, 0x200
	s_addc_u32 s11, s91, 0
	s_mov_b32 s28, 1
	s_branch .LBB0_1764

; __device__ __forceinline__ unsigned xb_ld(unsigned* p)              { return __hip_atomic_load(p, __ATOMIC_RELAXED, __HIP_MEMORY_SCOPE_AGENT); }
; __device__ __forceinline__ unsigned xb_add(unsigned* p, unsigned v) { return __hip_atomic_fetch_add(p, v, __ATOMIC_RELAXED, __HIP_MEMORY_SCOPE_AGENT); }
; #define XB_SPIN(cond, bar) do { unsigned _sp = 0; while (cond) { __builtin_amdgcn_s_sleep(1); \
;     if ((++_sp & 255u) == 0u) { if (xb_ld(&(bar)[XB_TMO])) break; if (_sp > XB_SPIN_CAP) { atomicAdd(&(bar)[XB_TMO], 1u); break; } } } } while (0)
; __device__ __forceinline__ void xcd_barrier(const XcdBarrier& b) {
;     ...
;         unsigned nloc = b.st[0], nx = b.st[1];
;         if (nloc == 0u) { xcd_barrier_complete(bar, b.x, nloc, nx); b.st[0] = nloc; b.st[1] = nx; }
;         const unsigned old = xb_add(&bar[XB_XSUB(b.x)], 1u);
;         const unsigned gen = old / nloc;
;         if (old + 1u == (gen + 1u) * nloc) {
;             __builtin_amdgcn_fence(__ATOMIC_RELEASE, "agent");
;             asm volatile("s_waitcnt vmcnt(0)" ::: "memory");
;             const unsigned og = xb_add(&bar[XB_TOP], 1u);
;             const unsigned tg = og / nx;
;             if (og + 1u == (tg + 1u) * nx) xb_add(&bar[XB_TOPGEN], 1u);
;             else XB_SPIN(xb_ld(&bar[XB_TOPGEN]) == tg, bar);
;             __builtin_amdgcn_fence(__ATOMIC_ACQUIRE, "agent");
;             xb_add(&bar[XB_XGEN(b.x)], 1u);
;             asm volatile("s_waitcnt vmcnt(0)" ::: "memory");
;         } else {
;             XB_SPIN(xb_ld(&bar[XB_XGEN(b.x)]) == gen, bar);
.LBB0_1826:
	s_or_b64 exec, exec, s[8:9]
	v_cvt_f32_u32_e32 v5, v3
	s_waitcnt vmcnt(0)
	v_readfirstlane_b32 s6, v4
	v_sub_u32_e32 v4, 0, v3
	v_rcp_iflag_f32_e32 v5, v5
	v_add_u32_e32 v6, s6, v2
	v_mul_f32_e32 v5, 0x4f7ffffe, v5
	v_cvt_u32_f32_e32 v5, v5
	v_mul_lo_u32 v2, v4, v5
	v_mul_hi_u32 v2, v5, v2
	v_add_u32_e32 v2, v5, v2
	v_mul_hi_u32 v2, v6, v2
	v_mul_lo_u32 v4, v2, v3
	v_sub_u32_e32 v4, v6, v4
	v_add_u32_e32 v5, 1, v2
	v_cmp_ge_u32_e32 vcc, v4, v3
	s_nop 1
	v_cndmask_b32_e32 v2, v2, v5, vcc
	v_sub_u32_e32 v5, v4, v3
	v_cndmask_b32_e32 v4, v4, v5, vcc
	v_add_u32_e32 v5, 1, v2
	v_cmp_ge_u32_e32 vcc, v4, v3
	v_add_u32_e32 v4, 1, v6
	s_nop 0
	v_cndmask_b32_e32 v2, v2, v5, vcc
	v_mul_lo_u32 v5, v3, v2
	v_add_u32_e32 v3, v5, v3
	v_cmp_ne_u32_e32 vcc, v4, v3
	s_and_saveexec_b64 s[6:7], vcc
	s_xor_b64 s[6:7], exec, s[6:7]
	s_cbranch_execz .LBB0_1840
	s_waitcnt lgkmcnt(0)
	buffer_inv sc1
	v_mov_b32_e32 v1, 0x2000
	global_load_dword v1, v1, s[2:3] offset:1024 sc1
	s_add_u32 s10, s2, 0x2400
	s_addc_u32 s11, s3, 0
	s_waitcnt vmcnt(0)
	v_cmp_eq_u32_e32 vcc, v1, v2
	s_and_saveexec_b64 s[8:9], vcc
	s_cbranch_execz .LBB0_1839
	s_mov_b32 s24, 1
	s_mov_b64 s[12:13], 0
	v_mov_b32_e32 v1, 0
	s_branch .LBB0_1830

; __device__ __forceinline__ unsigned xb_ld(unsigned* p)              { return __hip_atomic_load(p, __ATOMIC_RELAXED, __HIP_MEMORY_SCOPE_AGENT); }
; __device__ __forceinline__ unsigned xb_add(unsigned* p, unsigned v) { return __hip_atomic_fetch_add(p, v, __ATOMIC_RELAXED, __HIP_MEMORY_SCOPE_AGENT); }
; #define XB_SPIN(cond, bar) do { unsigned _sp = 0; while (cond) { __builtin_amdgcn_s_sleep(1); \
;     if ((++_sp & 255u) == 0u) { if (xb_ld(&(bar)[XB_TMO])) break; if (_sp > XB_SPIN_CAP) { atomicAdd(&(bar)[XB_TMO], 1u); break; } } } } while (0)
; __device__ __forceinline__ void xcd_barrier(const XcdBarrier& b) {
;     ...
;             const unsigned og = xb_add(&bar[XB_TOP], 1u);
;             const unsigned tg = og / nx;
;             if (og + 1u == (tg + 1u) * nx) xb_add(&bar[XB_TOPGEN], 1u);
;             else XB_SPIN(xb_ld(&bar[XB_TOPGEN]) == tg, bar);
.LBB0_1843:
	s_or_b64 exec, exec, s[8:9]
	buffer_inv sc1
	v_cvt_f32_u32_e32 v4, v1
	s_waitcnt vmcnt(0)
	v_readfirstlane_b32 s6, v3
	s_add_u32 s8, s90, 0x3500
	s_addc_u32 s9, s91, 0
	v_rcp_iflag_f32_e32 v4, v4
	v_add_u32_e32 v2, s6, v2
	v_add_u32_e32 v5, 1, v2
	s_mov_b64 s[10:11], -1
	v_mul_f32_e32 v3, 0x4f7ffffe, v4
	v_cvt_u32_f32_e32 v3, v3
	v_sub_u32_e32 v4, 0, v1
	v_mul_lo_u32 v4, v4, v3
	v_mul_hi_u32 v4, v3, v4
	v_add_u32_e32 v3, v3, v4
	v_mul_hi_u32 v3, v2, v3
	v_mul_lo_u32 v4, v3, v1
	v_sub_u32_e32 v2, v2, v4
	v_add_u32_e32 v6, 1, v3
	v_cmp_ge_u32_e32 vcc, v2, v1
	v_sub_u32_e32 v4, v2, v1
	s_nop 0
	v_cndmask_b32_e32 v3, v3, v6, vcc
	v_cndmask_b32_e32 v2, v2, v4, vcc
	v_add_u32_e32 v4, 1, v3
	v_cmp_ge_u32_e32 vcc, v2, v1
	s_nop 1
	v_cndmask_b32_e32 v4, v3, v4, vcc
	v_mul_lo_u32 v2, v1, v4
	v_add_u32_e32 v1, v2, v1
	v_cmp_ne_u32_e32 vcc, v5, v1
	v_mov_b64_e32 v[2:3], s[8:9]
	s_and_saveexec_b64 s[6:7], vcc
	s_cbranch_execz .LBB0_1855
	v_mov_b32_e32 v1, 0
	global_load_dword v2, v1, s[8:9] sc1
	s_mov_b64 s[14:15], 0
	s_waitcnt vmcnt(0)
	v_cmp_eq_u32_e32 vcc, v2, v4
	s_and_saveexec_b64 s[12:13], vcc
	s_cbranch_execz .LBB0_1854
	s_add_u32 s10, s90, 0x200
	s_addc_u32 s11, s91, 0
	s_mov_b32 s26, 1
	s_branch .LBB0_1847
